# P6 U sweep: gate (gelu) evaluation deferred to one vectorised pass over the 1024 entries after the sweep; per batch only z=k3*Es stored to LDS
# speedup vs baseline: 1.0132x; 1.0132x over previous
.Lp6a0_top:
	s_add_i32 s23, s23, 1
	s_add_i32 s2, s23, 3
	s_add_i32 s3, s22, -1
	s_min_i32 s2, s2, s3
	s_lshl_b32 s2, s2, 2
	s_add_i32 s2, s85, s2
	v_mov_b32_e32 v1, s2
	ds_read_b32 v252, v1 offset:4864
	s_and_b32 s2, s32, 0x3ff
	s_bfe_u32 s3, s32, 0x4000a
	v_cmp_gt_u32_e32 vcc, s3, v182
	s_lshl_b32 s2, s2, 2
	s_add_i32 s2, s2, s85
	v_cndmask_b32_e32 v1, 0, v182, vcc
	v_lshl_add_u32 v1, v1, 2, s2
	ds_read_b32 v1, v1 offset:8192
	s_and_b32 s2, s26, 0x3ff
	v_add_u32_e32 v210, s2, v180
	v_lshl_add_u32 v210, v210, 2, s85
	ds_read_b32 v196, v210
	s_waitcnt vmcnt(16)
	s_andn2_b64 vcc, exec, s[0:1]
	s_waitcnt lgkmcnt(0)
	v_readfirstlane_b32 s37, v252
	v_lshlrev_b32_e32 v1, 10, v1
	v_and_b32_e32 v1, 0x3fffc00, v1
	s_nop 0
	v_readlane_b32 s44, v1, 0
	v_readlane_b32 s45, v1, 1
	v_readlane_b32 s46, v1, 2
	v_readlane_b32 s47, v1, 3
	v_readlane_b32 s48, v1, 4
	v_readlane_b32 s49, v1, 5
	v_readlane_b32 s50, v1, 6
	v_readlane_b32 s51, v1, 7
	s_cbranch_vccnz .Lp6a0_954
	s_waitcnt vmcnt(8)
	v_lshlrev_b32_e32 v144, 16, v8
	v_and_b32_e32 v145, 0xffff0000, v8
	v_lshlrev_b32_e32 v146, 16, v9
	v_and_b32_e32 v147, 0xffff0000, v9
	v_lshlrev_b32_e32 v148, 16, v10
	v_and_b32_e32 v149, 0xffff0000, v10
	v_lshlrev_b32_e32 v150, 16, v11
	v_and_b32_e32 v151, 0xffff0000, v11
	v_lshlrev_b32_e32 v152, 16, v4
	v_and_b32_e32 v153, 0xffff0000, v4
	v_lshlrev_b32_e32 v154, 16, v5
	v_and_b32_e32 v155, 0xffff0000, v5
	v_lshlrev_b32_e32 v156, 16, v6
	v_and_b32_e32 v157, 0xffff0000, v6
	v_lshlrev_b32_e32 v158, 16, v7
	v_and_b32_e32 v159, 0xffff0000, v7

.Lp6a0_dotdone:
	s_nop 4
	buffer_load_dwordx4 v[68:71], v181, s[8:11], s44 offen
	buffer_load_dwordx4 v[64:67], v181, s[8:11], s45 offen
	buffer_load_dwordx4 v[60:63], v181, s[8:11], s46 offen
	buffer_load_dwordx4 v[56:59], v181, s[8:11], s47 offen
	buffer_load_dwordx4 v[48:51], v181, s[8:11], s48 offen
	buffer_load_dwordx4 v[32:35], v181, s[8:11], s49 offen
	buffer_load_dwordx4 v[16:19], v181, s[8:11], s50 offen
	buffer_load_dwordx4 v[12:15], v181, s[8:11], s51 offen
	v_permlane32_swap_b32_e32 v160, v168
	v_permlane32_swap_b32_e32 v162, v170
	v_permlane32_swap_b32_e32 v164, v172
	v_permlane32_swap_b32_e32 v166, v174
	v_add_f32_e32 v1, v160, v168
	v_add_f32_e32 v2, v162, v170
	v_add_f32_e32 v160, v164, v172
	v_add_f32_e32 v161, v166, v174
	s_nop 0
	v_permlane16_swap_b32_e32 v1, v160
	v_permlane16_swap_b32_e32 v2, v161
	v_add_f32_e32 v1, v1, v160
	v_add_f32_e32 v2, v2, v161
	v_cndmask_b32_e64 v160, v1, v2, s[4:5]
	v_cndmask_b32_e64 v1, v2, v1, s[4:5]
	s_bfe_u32 s14, s26, 0x4000a
	v_cmp_gt_u32_e32 vcc, s14, v180
	v_add_f32_dpp v1, v160, v1 row_ror:8 row_mask:0xf bank_mask:0xf bound_ctrl:1
	s_nop 1
	v_add_f32_dpp v1, v1, v1 row_half_mirror row_mask:0xf bank_mask:0xf bound_ctrl:1
	s_nop 1
	v_add_f32_dpp v2, v1, v1 quad_perm:[1,0,3,2] row_mask:0xf bank_mask:0xf bound_ctrl:1
	s_nop 1
	v_mov_b32_dpp v160, v2 quad_perm:[2,3,0,1] row_mask:0xf bank_mask:0xf bound_ctrl:1
	s_and_saveexec_b64 s[14:15], vcc
	v_add_f32_e32 v2, v2, v160
	v_mul_f32_e32 v1, v2, v196
	ds_write_b32 v210, v1
	s_or_b64 exec, exec, s[14:15]
	s_mov_b32 s26, s86
	s_mov_b32 s86, s27
	s_mov_b32 s27, s32
	s_mov_b32 s32, s37
	s_cmp_eq_u32 s22, s23
	s_cbranch_scc1 .Lp6_Adone

.Lp6a1_dotdone:
	s_nop 4
	buffer_load_dwordx4 v[72:75], v181, s[8:11], s44 offen
	buffer_load_dwordx4 v[52:55], v181, s[8:11], s45 offen
	buffer_load_dwordx4 v[44:47], v181, s[8:11], s46 offen
	buffer_load_dwordx4 v[40:43], v181, s[8:11], s47 offen
	buffer_load_dwordx4 v[36:39], v181, s[8:11], s48 offen
	buffer_load_dwordx4 v[28:31], v181, s[8:11], s49 offen
	buffer_load_dwordx4 v[24:27], v181, s[8:11], s50 offen
	buffer_load_dwordx4 v[20:23], v181, s[8:11], s51 offen
	v_permlane32_swap_b32_e32 v160, v168
	v_permlane32_swap_b32_e32 v162, v170
	v_permlane32_swap_b32_e32 v164, v172
	v_permlane32_swap_b32_e32 v166, v174
	v_add_f32_e32 v1, v160, v168
	v_add_f32_e32 v2, v162, v170
	v_add_f32_e32 v160, v164, v172
	v_add_f32_e32 v161, v166, v174
	s_nop 0
	v_permlane16_swap_b32_e32 v1, v160
	v_permlane16_swap_b32_e32 v2, v161
	v_add_f32_e32 v1, v1, v160
	v_add_f32_e32 v2, v2, v161
	v_cndmask_b32_e64 v160, v1, v2, s[4:5]
	v_cndmask_b32_e64 v1, v2, v1, s[4:5]
	s_bfe_u32 s14, s26, 0x4000a
	v_cmp_gt_u32_e32 vcc, s14, v180
	v_add_f32_dpp v1, v160, v1 row_ror:8 row_mask:0xf bank_mask:0xf bound_ctrl:1
	s_nop 1
	v_add_f32_dpp v1, v1, v1 row_half_mirror row_mask:0xf bank_mask:0xf bound_ctrl:1
	s_nop 1
	v_add_f32_dpp v2, v1, v1 quad_perm:[1,0,3,2] row_mask:0xf bank_mask:0xf bound_ctrl:1
	s_nop 1
	v_mov_b32_dpp v160, v2 quad_perm:[2,3,0,1] row_mask:0xf bank_mask:0xf bound_ctrl:1
	s_and_saveexec_b64 s[14:15], vcc
	v_add_f32_e32 v2, v2, v160
	v_mul_f32_e32 v1, v2, v196
	ds_write_b32 v210, v1
	s_or_b64 exec, exec, s[14:15]
	s_mov_b32 s26, s86
	s_mov_b32 s86, s27
	s_mov_b32 s27, s32
	s_mov_b32 s32, s37
	s_cmp_eq_u32 s22, s23
	s_cbranch_scc1 .Lp6_Adone

.Lp6a2_dotdone:
	s_nop 4
	buffer_load_dwordx4 v[224:227], v181, s[8:11], s44 offen
	buffer_load_dwordx4 v[228:231], v181, s[8:11], s45 offen
	buffer_load_dwordx4 v[232:235], v181, s[8:11], s46 offen
	buffer_load_dwordx4 v[236:239], v181, s[8:11], s47 offen
	buffer_load_dwordx4 v[240:243], v181, s[8:11], s48 offen
	buffer_load_dwordx4 v[244:247], v181, s[8:11], s49 offen
	buffer_load_dwordx4 v[248:251], v181, s[8:11], s50 offen
	buffer_load_dwordx4 v[216:219], v181, s[8:11], s51 offen
	v_permlane32_swap_b32_e32 v160, v168
	v_permlane32_swap_b32_e32 v162, v170
	v_permlane32_swap_b32_e32 v164, v172
	v_permlane32_swap_b32_e32 v166, v174
	v_add_f32_e32 v1, v160, v168
	v_add_f32_e32 v2, v162, v170
	v_add_f32_e32 v160, v164, v172
	v_add_f32_e32 v161, v166, v174
	s_nop 0
	v_permlane16_swap_b32_e32 v1, v160
	v_permlane16_swap_b32_e32 v2, v161
	v_add_f32_e32 v1, v1, v160
	v_add_f32_e32 v2, v2, v161
	v_cndmask_b32_e64 v160, v1, v2, s[4:5]
	v_cndmask_b32_e64 v1, v2, v1, s[4:5]
	s_bfe_u32 s14, s26, 0x4000a
	v_cmp_gt_u32_e32 vcc, s14, v180
	v_add_f32_dpp v1, v160, v1 row_ror:8 row_mask:0xf bank_mask:0xf bound_ctrl:1
	s_nop 1
	v_add_f32_dpp v1, v1, v1 row_half_mirror row_mask:0xf bank_mask:0xf bound_ctrl:1
	s_nop 1
	v_add_f32_dpp v2, v1, v1 quad_perm:[1,0,3,2] row_mask:0xf bank_mask:0xf bound_ctrl:1
	s_nop 1
	v_mov_b32_dpp v160, v2 quad_perm:[2,3,0,1] row_mask:0xf bank_mask:0xf bound_ctrl:1
	s_and_saveexec_b64 s[14:15], vcc
	v_add_f32_e32 v2, v2, v160
	v_mul_f32_e32 v1, v2, v196
	ds_write_b32 v210, v1
	s_or_b64 exec, exec, s[14:15]
	s_mov_b32 s26, s86
	s_mov_b32 s86, s27
	s_mov_b32 s27, s32
	s_mov_b32 s32, s37
	s_cmp_eq_u32 s22, s23
	s_cbranch_scc1 .Lp6_Adone
	s_branch .Lp6a0_top
.Lp6_Adone:
	s_waitcnt vmcnt(0)
	v_lshl_add_u32 v210, v178, 2, s85
	s_mov_b32 s26, 0x3e6d3388
	ds_read_b32 v12, v210 offset:0
	ds_read_b32 v13, v210 offset:12288
	ds_read_b32 v14, v210 offset:256
	ds_read_b32 v15, v210 offset:12544
	ds_read_b32 v16, v210 offset:512
	ds_read_b32 v17, v210 offset:12800
	ds_read_b32 v18, v210 offset:768
	ds_read_b32 v19, v210 offset:13056
	ds_read_b32 v20, v210 offset:1024
	ds_read_b32 v21, v210 offset:13312
	ds_read_b32 v22, v210 offset:1280
	ds_read_b32 v23, v210 offset:13568
	ds_read_b32 v24, v210 offset:1536
	ds_read_b32 v25, v210 offset:13824
	ds_read_b32 v26, v210 offset:1792
	ds_read_b32 v27, v210 offset:14080
	s_waitcnt lgkmcnt(14)
	v_fma_f32 v2, |v12|, s26, 1.0
	v_rcp_f32_e32 v2, v2
	v_mov_b32_e32 v160, 0xbf3a00e3
	v_cmp_gt_f32_e32 vcc, 0, v12
	v_fmamk_f32 v160, v2, 0x3f07dc22, v160
	v_fmaak_f32 v160, v2, v160, 0x3f35f0e3
	v_fmaak_f32 v160, v2, v160, 0xbe11a98e
	v_fmaak_f32 v160, v2, v160, 0x3e027906
	v_mul_f32_e32 v2, v2, v160
	v_mul_f32_e32 v160, v12, v12
	v_mul_f32_e32 v160, 0xbf38aa3b, v160
	v_exp_f32_e32 v160, v160
	s_nop 0
	v_mul_f32_e32 v2, v160, v2
	v_mul_f32_e32 v160, v12, v2
	v_fma_f32 v1, -v12, v2, v12
	v_cndmask_b32_e32 v1, v1, v160, vcc
	v_mul_f32_e32 v1, v13, v1
	ds_write_b32 v210, v1 offset:12288
	s_waitcnt lgkmcnt(13)
	v_fma_f32 v2, |v14|, s26, 1.0
	v_rcp_f32_e32 v2, v2
	v_mov_b32_e32 v160, 0xbf3a00e3
	v_cmp_gt_f32_e32 vcc, 0, v14
	v_fmamk_f32 v160, v2, 0x3f07dc22, v160
	v_fmaak_f32 v160, v2, v160, 0x3f35f0e3
	v_fmaak_f32 v160, v2, v160, 0xbe11a98e
	v_fmaak_f32 v160, v2, v160, 0x3e027906
	v_mul_f32_e32 v2, v2, v160
	v_mul_f32_e32 v160, v14, v14
	v_mul_f32_e32 v160, 0xbf38aa3b, v160
	v_exp_f32_e32 v160, v160
	s_nop 0
	v_mul_f32_e32 v2, v160, v2
	v_mul_f32_e32 v160, v14, v2
	v_fma_f32 v1, -v14, v2, v14
	v_cndmask_b32_e32 v1, v1, v160, vcc
	v_mul_f32_e32 v1, v15, v1
	ds_write_b32 v210, v1 offset:12544
	s_waitcnt lgkmcnt(12)
	v_fma_f32 v2, |v16|, s26, 1.0
	v_rcp_f32_e32 v2, v2
	v_mov_b32_e32 v160, 0xbf3a00e3
	v_cmp_gt_f32_e32 vcc, 0, v16
	v_fmamk_f32 v160, v2, 0x3f07dc22, v160
	v_fmaak_f32 v160, v2, v160, 0x3f35f0e3
	v_fmaak_f32 v160, v2, v160, 0xbe11a98e
	v_fmaak_f32 v160, v2, v160, 0x3e027906
	v_mul_f32_e32 v2, v2, v160
	v_mul_f32_e32 v160, v16, v16
	v_mul_f32_e32 v160, 0xbf38aa3b, v160
	v_exp_f32_e32 v160, v160
	s_nop 0
	v_mul_f32_e32 v2, v160, v2
	v_mul_f32_e32 v160, v16, v2
	v_fma_f32 v1, -v16, v2, v16
	v_cndmask_b32_e32 v1, v1, v160, vcc
	v_mul_f32_e32 v1, v17, v1
	ds_write_b32 v210, v1 offset:12800
	s_waitcnt lgkmcnt(11)
	v_fma_f32 v2, |v18|, s26, 1.0
	v_rcp_f32_e32 v2, v2
	v_mov_b32_e32 v160, 0xbf3a00e3
	v_cmp_gt_f32_e32 vcc, 0, v18
	v_fmamk_f32 v160, v2, 0x3f07dc22, v160
	v_fmaak_f32 v160, v2, v160, 0x3f35f0e3
	v_fmaak_f32 v160, v2, v160, 0xbe11a98e
	v_fmaak_f32 v160, v2, v160, 0x3e027906
	v_mul_f32_e32 v2, v2, v160
	v_mul_f32_e32 v160, v18, v18
	v_mul_f32_e32 v160, 0xbf38aa3b, v160
	v_exp_f32_e32 v160, v160
	s_nop 0
	v_mul_f32_e32 v2, v160, v2
	v_mul_f32_e32 v160, v18, v2
	v_fma_f32 v1, -v18, v2, v18
	v_cndmask_b32_e32 v1, v1, v160, vcc
	v_mul_f32_e32 v1, v19, v1
	ds_write_b32 v210, v1 offset:13056
	s_waitcnt lgkmcnt(10)
	v_fma_f32 v2, |v20|, s26, 1.0
	v_rcp_f32_e32 v2, v2
	v_mov_b32_e32 v160, 0xbf3a00e3
	v_cmp_gt_f32_e32 vcc, 0, v20
	v_fmamk_f32 v160, v2, 0x3f07dc22, v160
	v_fmaak_f32 v160, v2, v160, 0x3f35f0e3
	v_fmaak_f32 v160, v2, v160, 0xbe11a98e
	v_fmaak_f32 v160, v2, v160, 0x3e027906
	v_mul_f32_e32 v2, v2, v160
	v_mul_f32_e32 v160, v20, v20
	v_mul_f32_e32 v160, 0xbf38aa3b, v160
	v_exp_f32_e32 v160, v160
	s_nop 0
	v_mul_f32_e32 v2, v160, v2
	v_mul_f32_e32 v160, v20, v2
	v_fma_f32 v1, -v20, v2, v20
	v_cndmask_b32_e32 v1, v1, v160, vcc
	v_mul_f32_e32 v1, v21, v1
	ds_write_b32 v210, v1 offset:13312
	s_waitcnt lgkmcnt(9)
	v_fma_f32 v2, |v22|, s26, 1.0
	v_rcp_f32_e32 v2, v2
	v_mov_b32_e32 v160, 0xbf3a00e3
	v_cmp_gt_f32_e32 vcc, 0, v22
	v_fmamk_f32 v160, v2, 0x3f07dc22, v160
	v_fmaak_f32 v160, v2, v160, 0x3f35f0e3
	v_fmaak_f32 v160, v2, v160, 0xbe11a98e
	v_fmaak_f32 v160, v2, v160, 0x3e027906
	v_mul_f32_e32 v2, v2, v160
	v_mul_f32_e32 v160, v22, v22
	v_mul_f32_e32 v160, 0xbf38aa3b, v160
	v_exp_f32_e32 v160, v160
	s_nop 0
	v_mul_f32_e32 v2, v160, v2
	v_mul_f32_e32 v160, v22, v2
	v_fma_f32 v1, -v22, v2, v22
	v_cndmask_b32_e32 v1, v1, v160, vcc
	v_mul_f32_e32 v1, v23, v1
	ds_write_b32 v210, v1 offset:13568
	s_waitcnt lgkmcnt(8)
	v_fma_f32 v2, |v24|, s26, 1.0
	v_rcp_f32_e32 v2, v2
	v_mov_b32_e32 v160, 0xbf3a00e3
	v_cmp_gt_f32_e32 vcc, 0, v24
	v_fmamk_f32 v160, v2, 0x3f07dc22, v160
	v_fmaak_f32 v160, v2, v160, 0x3f35f0e3
	v_fmaak_f32 v160, v2, v160, 0xbe11a98e
	v_fmaak_f32 v160, v2, v160, 0x3e027906
	v_mul_f32_e32 v2, v2, v160
	v_mul_f32_e32 v160, v24, v24
	v_mul_f32_e32 v160, 0xbf38aa3b, v160
	v_exp_f32_e32 v160, v160
	s_nop 0
	v_mul_f32_e32 v2, v160, v2
	v_mul_f32_e32 v160, v24, v2
	v_fma_f32 v1, -v24, v2, v24
	v_cndmask_b32_e32 v1, v1, v160, vcc
	v_mul_f32_e32 v1, v25, v1
	ds_write_b32 v210, v1 offset:13824
	s_waitcnt lgkmcnt(7)
	v_fma_f32 v2, |v26|, s26, 1.0
	v_rcp_f32_e32 v2, v2
	v_mov_b32_e32 v160, 0xbf3a00e3
	v_cmp_gt_f32_e32 vcc, 0, v26
	v_fmamk_f32 v160, v2, 0x3f07dc22, v160
	v_fmaak_f32 v160, v2, v160, 0x3f35f0e3
	v_fmaak_f32 v160, v2, v160, 0xbe11a98e
	v_fmaak_f32 v160, v2, v160, 0x3e027906
	v_mul_f32_e32 v2, v2, v160
	v_mul_f32_e32 v160, v26, v26
	v_mul_f32_e32 v160, 0xbf38aa3b, v160
	v_exp_f32_e32 v160, v160
	s_nop 0
	v_mul_f32_e32 v2, v160, v2
	v_mul_f32_e32 v160, v26, v2
	v_fma_f32 v1, -v26, v2, v26
	v_cndmask_b32_e32 v1, v1, v160, vcc
	v_mul_f32_e32 v1, v27, v1
	ds_write_b32 v210, v1 offset:14080
	ds_read_b32 v12, v210 offset:2048
	ds_read_b32 v13, v210 offset:14336
	ds_read_b32 v14, v210 offset:2304
	ds_read_b32 v15, v210 offset:14592
	ds_read_b32 v16, v210 offset:2560
	ds_read_b32 v17, v210 offset:14848
	ds_read_b32 v18, v210 offset:2816
	ds_read_b32 v19, v210 offset:15104
	ds_read_b32 v20, v210 offset:3072
	ds_read_b32 v21, v210 offset:15360
	ds_read_b32 v22, v210 offset:3328
	ds_read_b32 v23, v210 offset:15616
	ds_read_b32 v24, v210 offset:3584
	ds_read_b32 v25, v210 offset:15872
	ds_read_b32 v26, v210 offset:3840
	ds_read_b32 v27, v210 offset:16128
	s_waitcnt lgkmcnt(14)
	v_fma_f32 v2, |v12|, s26, 1.0
	v_rcp_f32_e32 v2, v2
	v_mov_b32_e32 v160, 0xbf3a00e3
	v_cmp_gt_f32_e32 vcc, 0, v12
	v_fmamk_f32 v160, v2, 0x3f07dc22, v160
	v_fmaak_f32 v160, v2, v160, 0x3f35f0e3
	v_fmaak_f32 v160, v2, v160, 0xbe11a98e
	v_fmaak_f32 v160, v2, v160, 0x3e027906
	v_mul_f32_e32 v2, v2, v160
	v_mul_f32_e32 v160, v12, v12
	v_mul_f32_e32 v160, 0xbf38aa3b, v160
	v_exp_f32_e32 v160, v160
	s_nop 0
	v_mul_f32_e32 v2, v160, v2
	v_mul_f32_e32 v160, v12, v2
	v_fma_f32 v1, -v12, v2, v12
	v_cndmask_b32_e32 v1, v1, v160, vcc
	v_mul_f32_e32 v1, v13, v1
	ds_write_b32 v210, v1 offset:14336
	s_waitcnt lgkmcnt(13)
	v_fma_f32 v2, |v14|, s26, 1.0
	v_rcp_f32_e32 v2, v2
	v_mov_b32_e32 v160, 0xbf3a00e3
	v_cmp_gt_f32_e32 vcc, 0, v14
	v_fmamk_f32 v160, v2, 0x3f07dc22, v160
	v_fmaak_f32 v160, v2, v160, 0x3f35f0e3
	v_fmaak_f32 v160, v2, v160, 0xbe11a98e
	v_fmaak_f32 v160, v2, v160, 0x3e027906
	v_mul_f32_e32 v2, v2, v160
	v_mul_f32_e32 v160, v14, v14
	v_mul_f32_e32 v160, 0xbf38aa3b, v160
	v_exp_f32_e32 v160, v160
	s_nop 0
	v_mul_f32_e32 v2, v160, v2
	v_mul_f32_e32 v160, v14, v2
	v_fma_f32 v1, -v14, v2, v14
	v_cndmask_b32_e32 v1, v1, v160, vcc
	v_mul_f32_e32 v1, v15, v1
	ds_write_b32 v210, v1 offset:14592
	s_waitcnt lgkmcnt(12)
	v_fma_f32 v2, |v16|, s26, 1.0
	v_rcp_f32_e32 v2, v2
	v_mov_b32_e32 v160, 0xbf3a00e3
	v_cmp_gt_f32_e32 vcc, 0, v16
	v_fmamk_f32 v160, v2, 0x3f07dc22, v160
	v_fmaak_f32 v160, v2, v160, 0x3f35f0e3
	v_fmaak_f32 v160, v2, v160, 0xbe11a98e
	v_fmaak_f32 v160, v2, v160, 0x3e027906
	v_mul_f32_e32 v2, v2, v160
	v_mul_f32_e32 v160, v16, v16
	v_mul_f32_e32 v160, 0xbf38aa3b, v160
	v_exp_f32_e32 v160, v160
	s_nop 0
	v_mul_f32_e32 v2, v160, v2
	v_mul_f32_e32 v160, v16, v2
	v_fma_f32 v1, -v16, v2, v16
	v_cndmask_b32_e32 v1, v1, v160, vcc
	v_mul_f32_e32 v1, v17, v1
	ds_write_b32 v210, v1 offset:14848
	s_waitcnt lgkmcnt(11)
	v_fma_f32 v2, |v18|, s26, 1.0
	v_rcp_f32_e32 v2, v2
	v_mov_b32_e32 v160, 0xbf3a00e3
	v_cmp_gt_f32_e32 vcc, 0, v18
	v_fmamk_f32 v160, v2, 0x3f07dc22, v160
	v_fmaak_f32 v160, v2, v160, 0x3f35f0e3
	v_fmaak_f32 v160, v2, v160, 0xbe11a98e
	v_fmaak_f32 v160, v2, v160, 0x3e027906
	v_mul_f32_e32 v2, v2, v160
	v_mul_f32_e32 v160, v18, v18
	v_mul_f32_e32 v160, 0xbf38aa3b, v160
	v_exp_f32_e32 v160, v160
	s_nop 0
	v_mul_f32_e32 v2, v160, v2
	v_mul_f32_e32 v160, v18, v2
	v_fma_f32 v1, -v18, v2, v18
	v_cndmask_b32_e32 v1, v1, v160, vcc
	v_mul_f32_e32 v1, v19, v1
	ds_write_b32 v210, v1 offset:15104
	s_waitcnt lgkmcnt(10)
	v_fma_f32 v2, |v20|, s26, 1.0
	v_rcp_f32_e32 v2, v2
	v_mov_b32_e32 v160, 0xbf3a00e3
	v_cmp_gt_f32_e32 vcc, 0, v20
	v_fmamk_f32 v160, v2, 0x3f07dc22, v160
	v_fmaak_f32 v160, v2, v160, 0x3f35f0e3
	v_fmaak_f32 v160, v2, v160, 0xbe11a98e
	v_fmaak_f32 v160, v2, v160, 0x3e027906
	v_mul_f32_e32 v2, v2, v160
	v_mul_f32_e32 v160, v20, v20
	v_mul_f32_e32 v160, 0xbf38aa3b, v160
	v_exp_f32_e32 v160, v160
	s_nop 0
	v_mul_f32_e32 v2, v160, v2
	v_mul_f32_e32 v160, v20, v2
	v_fma_f32 v1, -v20, v2, v20
	v_cndmask_b32_e32 v1, v1, v160, vcc
	v_mul_f32_e32 v1, v21, v1
	ds_write_b32 v210, v1 offset:15360
	s_waitcnt lgkmcnt(9)
	v_fma_f32 v2, |v22|, s26, 1.0
	v_rcp_f32_e32 v2, v2
	v_mov_b32_e32 v160, 0xbf3a00e3
	v_cmp_gt_f32_e32 vcc, 0, v22
	v_fmamk_f32 v160, v2, 0x3f07dc22, v160
	v_fmaak_f32 v160, v2, v160, 0x3f35f0e3
	v_fmaak_f32 v160, v2, v160, 0xbe11a98e
	v_fmaak_f32 v160, v2, v160, 0x3e027906
	v_mul_f32_e32 v2, v2, v160
	v_mul_f32_e32 v160, v22, v22
	v_mul_f32_e32 v160, 0xbf38aa3b, v160
	v_exp_f32_e32 v160, v160
	s_nop 0
	v_mul_f32_e32 v2, v160, v2
	v_mul_f32_e32 v160, v22, v2
	v_fma_f32 v1, -v22, v2, v22
	v_cndmask_b32_e32 v1, v1, v160, vcc
	v_mul_f32_e32 v1, v23, v1
	ds_write_b32 v210, v1 offset:15616
	s_waitcnt lgkmcnt(8)
	v_fma_f32 v2, |v24|, s26, 1.0
	v_rcp_f32_e32 v2, v2
	v_mov_b32_e32 v160, 0xbf3a00e3
	v_cmp_gt_f32_e32 vcc, 0, v24
	v_fmamk_f32 v160, v2, 0x3f07dc22, v160
	v_fmaak_f32 v160, v2, v160, 0x3f35f0e3
	v_fmaak_f32 v160, v2, v160, 0xbe11a98e
	v_fmaak_f32 v160, v2, v160, 0x3e027906
	v_mul_f32_e32 v2, v2, v160
	v_mul_f32_e32 v160, v24, v24
	v_mul_f32_e32 v160, 0xbf38aa3b, v160
	v_exp_f32_e32 v160, v160
	s_nop 0
	v_mul_f32_e32 v2, v160, v2
	v_mul_f32_e32 v160, v24, v2
	v_fma_f32 v1, -v24, v2, v24
	v_cndmask_b32_e32 v1, v1, v160, vcc
	v_mul_f32_e32 v1, v25, v1
	ds_write_b32 v210, v1 offset:15872
	s_waitcnt lgkmcnt(7)
	v_fma_f32 v2, |v26|, s26, 1.0
	v_rcp_f32_e32 v2, v2
	v_mov_b32_e32 v160, 0xbf3a00e3
	v_cmp_gt_f32_e32 vcc, 0, v26
	v_fmamk_f32 v160, v2, 0x3f07dc22, v160
	v_fmaak_f32 v160, v2, v160, 0x3f35f0e3
	v_fmaak_f32 v160, v2, v160, 0xbe11a98e
	v_fmaak_f32 v160, v2, v160, 0x3e027906
	v_mul_f32_e32 v2, v2, v160
	v_mul_f32_e32 v160, v26, v26
	v_mul_f32_e32 v160, 0xbf38aa3b, v160
	v_exp_f32_e32 v160, v160
	s_nop 0
	v_mul_f32_e32 v2, v160, v2
	v_mul_f32_e32 v160, v26, v2
	v_fma_f32 v1, -v26, v2, v26
	v_cndmask_b32_e32 v1, v1, v160, vcc
	v_mul_f32_e32 v1, v27, v1
	ds_write_b32 v210, v1 offset:16128
	s_waitcnt lgkmcnt(0)
	v_mov_b32_e32 v184, 0
	v_mov_b32_e32 v185, 0
	v_mov_b64_e32 v[126:127], v[184:185]
	v_mov_b64_e32 v[128:129], v[184:185]
	v_mov_b64_e32 v[130:131], v[184:185]
	v_mov_b64_e32 v[132:133], v[184:185]
	v_mov_b64_e32 v[134:135], v[184:185]
	v_mov_b64_e32 v[136:137], v[184:185]
	v_mov_b64_e32 v[138:139], v[184:185]
	v_mov_b64_e32 v[140:141], v[184:185]
	v_mov_b64_e32 v[110:111], v[184:185]
	v_mov_b64_e32 v[112:113], v[184:185]
	v_mov_b64_e32 v[114:115], v[184:185]
	v_mov_b64_e32 v[116:117], v[184:185]
	v_mov_b64_e32 v[118:119], v[184:185]
	v_mov_b64_e32 v[120:121], v[184:185]
	v_mov_b64_e32 v[122:123], v[184:185]
	v_mov_b64_e32 v[124:125], v[184:185]
	v_mov_b64_e32 v[94:95], v[184:185]
	v_mov_b64_e32 v[96:97], v[184:185]
	v_mov_b64_e32 v[98:99], v[184:185]
	v_mov_b64_e32 v[100:101], v[184:185]
	v_mov_b64_e32 v[102:103], v[184:185]
	v_mov_b64_e32 v[104:105], v[184:185]
	v_mov_b64_e32 v[106:107], v[184:185]
	v_mov_b64_e32 v[108:109], v[184:185]
	v_mov_b64_e32 v[78:79], v[184:185]
	v_mov_b64_e32 v[80:81], v[184:185]
	v_mov_b64_e32 v[82:83], v[184:185]
	v_mov_b64_e32 v[86:87], v[184:185]
	v_mov_b64_e32 v[88:89], v[184:185]
	v_mov_b64_e32 v[90:91], v[184:185]
	v_mov_b64_e32 v[92:93], v[184:185]
	v_mov_b64_e32 v[84:85], v[184:185]
	v_mov_b64_e32 v[144:145], v[184:185]
	v_mov_b64_e32 v[146:147], v[184:185]
	v_mov_b64_e32 v[148:149], v[184:185]
	v_mov_b64_e32 v[150:151], v[184:185]
	v_mov_b64_e32 v[152:153], v[184:185]
	v_mov_b64_e32 v[154:155], v[184:185]
	v_mov_b64_e32 v[156:157], v[184:185]
	v_mov_b64_e32 v[158:159], v[184:185]
	v_mov_b64_e32 v[160:161], v[184:185]
	v_mov_b64_e32 v[162:163], v[184:185]
	v_mov_b64_e32 v[164:165], v[184:185]
	v_mov_b64_e32 v[166:167], v[184:185]
	v_mov_b64_e32 v[168:169], v[184:185]
	v_mov_b64_e32 v[170:171], v[184:185]
	v_mov_b64_e32 v[172:173], v[184:185]
	v_mov_b64_e32 v[174:175], v[184:185]
	v_mov_b64_e32 v[224:225], v[184:185]
	v_mov_b64_e32 v[226:227], v[184:185]
	v_mov_b64_e32 v[228:229], v[184:185]
	v_mov_b64_e32 v[230:231], v[184:185]
	v_mov_b64_e32 v[232:233], v[184:185]
	v_mov_b64_e32 v[234:235], v[184:185]
	v_mov_b64_e32 v[236:237], v[184:185]
	v_mov_b64_e32 v[238:239], v[184:185]
	v_mov_b64_e32 v[240:241], v[184:185]
	v_mov_b64_e32 v[242:243], v[184:185]
	v_mov_b64_e32 v[244:245], v[184:185]
	v_mov_b64_e32 v[246:247], v[184:185]
	v_mov_b64_e32 v[248:249], v[184:185]
	v_mov_b64_e32 v[250:251], v[184:185]
	v_mov_b64_e32 v[216:217], v[184:185]
	v_mov_b64_e32 v[218:219], v[184:185]
	s_add_i32 s3, s22, -1
	s_min_i32 s2, s3, 0
	s_max_i32 s2, s2, 0
	s_lshl_b32 s2, s2, 2
	s_add_i32 s2, s85, s2
	v_mov_b32_e32 v1, s2
	ds_read_b32 v1, v1 offset:4864
	s_waitcnt lgkmcnt(0)
	v_readfirstlane_b32 s26, v1
	s_and_b32 s2, s26, 0x3ff
	s_bfe_u32 s3, s26, 0x4000a
	v_cmp_gt_u32_e32 vcc, s3, v182
	s_lshl_b32 s2, s2, 2
	s_add_i32 s2, s2, s85
	v_cndmask_b32_e32 v1, 0, v182, vcc
	v_lshl_add_u32 v1, v1, 2, s2
	ds_read_b32 v1, v1 offset:8192
	s_waitcnt lgkmcnt(0)
	v_lshlrev_b32_e32 v1, 10, v1
	v_and_b32_e32 v1, 0x3fffc00, v1
	s_nop 0
	v_readlane_b32 s44, v1, 0
	v_readlane_b32 s45, v1, 1
	v_readlane_b32 s46, v1, 2
	v_readlane_b32 s47, v1, 3
	v_readlane_b32 s48, v1, 4
	v_readlane_b32 s49, v1, 5
	v_readlane_b32 s50, v1, 6
	v_readlane_b32 s51, v1, 7
	s_nop 4
	buffer_load_dwordx4 v[68:71], v181, s[92:95], s44 offen
	buffer_load_dwordx4 v[64:67], v181, s[92:95], s45 offen
	buffer_load_dwordx4 v[60:63], v181, s[92:95], s46 offen
	buffer_load_dwordx4 v[56:59], v181, s[92:95], s47 offen
	buffer_load_dwordx4 v[48:51], v181, s[92:95], s48 offen
	buffer_load_dwordx4 v[32:35], v181, s[92:95], s49 offen
	buffer_load_dwordx4 v[16:19], v181, s[92:95], s50 offen
	buffer_load_dwordx4 v[12:15], v181, s[92:95], s51 offen
	s_add_i32 s3, s22, -1
	s_min_i32 s2, s3, 1
	s_max_i32 s2, s2, 0
	s_lshl_b32 s2, s2, 2
	s_add_i32 s2, s85, s2
	v_mov_b32_e32 v1, s2
	ds_read_b32 v1, v1 offset:4864
	s_waitcnt lgkmcnt(0)
	v_readfirstlane_b32 s86, v1
	s_and_b32 s2, s86, 0x3ff
	s_bfe_u32 s3, s86, 0x4000a
	v_cmp_gt_u32_e32 vcc, s3, v182
	s_lshl_b32 s2, s2, 2
	s_add_i32 s2, s2, s85
	v_cndmask_b32_e32 v1, 0, v182, vcc
	v_lshl_add_u32 v1, v1, 2, s2
	ds_read_b32 v1, v1 offset:8192
	s_waitcnt lgkmcnt(0)
	v_lshlrev_b32_e32 v1, 10, v1
	v_and_b32_e32 v1, 0x3fffc00, v1
	s_nop 0
	v_readlane_b32 s44, v1, 0
	v_readlane_b32 s45, v1, 1
	v_readlane_b32 s46, v1, 2
	v_readlane_b32 s47, v1, 3
	v_readlane_b32 s48, v1, 4
	v_readlane_b32 s49, v1, 5
	v_readlane_b32 s50, v1, 6
	v_readlane_b32 s51, v1, 7
	s_nop 4
	buffer_load_dwordx4 v[72:75], v181, s[92:95], s44 offen
	buffer_load_dwordx4 v[52:55], v181, s[92:95], s45 offen
	buffer_load_dwordx4 v[44:47], v181, s[92:95], s46 offen
	buffer_load_dwordx4 v[40:43], v181, s[92:95], s47 offen
	buffer_load_dwordx4 v[36:39], v181, s[92:95], s48 offen
	buffer_load_dwordx4 v[28:31], v181, s[92:95], s49 offen
	buffer_load_dwordx4 v[24:27], v181, s[92:95], s50 offen
	buffer_load_dwordx4 v[20:23], v181, s[92:95], s51 offen
	s_add_i32 s3, s22, -1
	s_min_i32 s2, s3, 2
	s_max_i32 s2, s2, 0
	s_lshl_b32 s2, s2, 2
	s_add_i32 s2, s85, s2
	v_mov_b32_e32 v1, s2
	ds_read_b32 v1, v1 offset:4864
	s_waitcnt lgkmcnt(0)
	v_readfirstlane_b32 s32, v1
	s_mov_b32 s23, 0
